# conv1: pseudo-random per-CU/TG start delay in first dispatch round (breaks chip-wide lockstep); VQ waves 4-7 stagger; recfin odd-TG stagger; c2 deeper weight prefetch; proj preload
# speedup vs baseline: 1.0164x; 1.0051x over previous
_Z11k_conv1_t14I3GeoILi64ELi16ELi3ELi2EEEvPKfPKDv8_DF16_S3_Pfiiii:
	s_cmp_lt_u32 s4, 4
	s_cbranch_scc0 .Lc1_nosleep
	s_getreg_b32 s60, hwreg(HW_REG_HW_ID, 8, 12)
	s_mul_i32 s60, s60, 0x9e3b
	s_lshr_b32 s60, s60, 7
	s_and_b32 s60, s60, 31
	s_cmp_eq_u32 s60, 0
	s_cbranch_scc1 .Lc1_nosleep
.Lc1_sleep:
	s_sleep 4
	s_add_i32 s60, s60, -1
	s_cmp_lg_u32 s60, 0
	s_cbranch_scc1 .Lc1_sleep

_Z12k_recfin_t14I3GeoILi128ELi32ELi3ELi1EEEvPKfPKiPKDv8_DF16_S3_S8_S3_Pfiiii:
	s_getreg_b32 s60, hwreg(HW_REG_HW_ID, 16, 4)
	s_and_b32 s60, s60, 1
	s_cmp_eq_u32 s60, 0
	s_cbranch_scc1 .Lrf_nosleep
	s_sleep 30
.Lrf_nosleep:
	s_lshl_b32 s5, s2, 5
	s_movk_i32 s2, 0x330
	v_mul_u32_u24_e32 v1, 0x1e2, v0
	s_load_dwordx2 s[34:35], s[0:1], 0x8
	s_load_dwordx4 s[16:19], s[0:1], 0x38
	s_lshl_b32 s20, s3, 2
	v_lshrrev_b32_e32 v1, 16, v1
	v_cmp_gt_u32_e64 s[8:9], s2, v0
	s_add_i32 s33, s20, -1
	s_add_i32 s21, s5, -1
	v_cndmask_b32_e64 v2, 5, v1, s[8:9]
	v_add_u32_e32 v3, s33, v2
	v_cmp_lt_i32_e32 vcc, -1, v3
	s_and_b64 s[2:3], s[8:9], vcc
	s_mov_b64 s[26:27], -1
	v_lshrrev_b32_e32 v2, 2, v0
	s_mov_b64 s[28:29], -1
	s_and_saveexec_b64 s[10:11], s[2:3]
	s_cbranch_execz .LBB6_2
	v_mul_lo_u16_e32 v4, 31, v2
	v_lshrrev_b16_e32 v4, 10, v4
	v_mul_lo_u16_e32 v4, 34, v4
	v_sub_u16_e32 v4, v2, v4
	v_add_u32_sdwa v4, s21, v4 dst_sel:DWORD dst_unused:UNUSED_PAD src0_sel:DWORD src1_sel:BYTE_0
	v_cmp_gt_i32_e64 s[2:3], 0, v4
	s_waitcnt lgkmcnt(0)
	v_cmp_le_i32_e64 s[6:7], s17, v4
	v_cmp_le_i32_e32 vcc, s16, v3
	s_or_b64 s[2:3], s[2:3], s[6:7]
	s_or_b64 s[2:3], vcc, s[2:3]
	s_orn2_b64 s[28:29], s[2:3], exec
